# v069
# baseline (speedup 1.0000x reference)
_Z10gru_kernelPKhPf:
	s_load_dwordx4 s[8:11], s[0:1], 0x0
	s_lshr_b32 s20, s2, 1
	s_and_b32 s20, s20, 0x7fffffc
	s_and_b32 s21, s2, 3
	s_or_b32 s20, s20, s21
	s_lshl_b32 s20, s20, 12
	s_add_u32 s20, s20, 0x49000
	v_lshlrev_b32_e32 v249, 3, v0
	s_waitcnt lgkmcnt(0)
	s_add_u32 s20, s8, s20
	s_addc_u32 s21, s9, 0
	global_load_dwordx2 v[250:251], v249, s[20:21]
	s_movk_i32 s0, 0x200
	v_cmp_gt_u32_e32 vcc, s0, v0
	s_and_saveexec_b64 s[0:1], vcc
	s_cbranch_execz .LBB1_2
	v_mov_b32_e32 v2, 0
	v_lshlrev_b32_e32 v1, 4, v0
	v_mov_b32_e32 v3, v2
	v_mov_b32_e32 v4, v2
	v_mov_b32_e32 v5, v2
	ds_write_b128 v1, v[2:5]

.LBB1_8:
	s_or_b64 exec, exec, s[12:13]
	s_mov_b32 s14, 0
	v_cmp_eq_u32_e32 vcc, 0, v0
	s_and_saveexec_b64 s[0:1], vcc
	v_mov_b32_e32 v1, 0
	ds_write_b32 v1, v1 offset:24832
	s_or_b64 exec, exec, s[0:1]
	s_lshr_b32 s0, s2, 1
	s_and_b32 s0, s0, 0x7fffffc
	s_and_b32 s1, s2, 3
	s_or_b32 s0, s0, s1
	s_bfe_u32 s16, s2, 0x10002
	s_lshl_b32 s2, s0, 5
	s_ashr_i32 s3, s2, 31
	s_lshl_b64 s[0:1], s[2:3], 7
	s_waitcnt lgkmcnt(0)
	s_add_u32 s0, s8, s0
	s_addc_u32 s1, s9, s1
	s_add_u32 s4, s0, 0x49000
	s_addc_u32 s5, s1, 0
	v_add_u32_e32 v5, 1, v2
	s_cmp_eq_u32 s16, 0
	v_lshlrev_b32_e32 v1, 9, v5
	s_cselect_b64 vcc, -1, 0
	v_add_u32_e32 v2, 0x4080, v6
	v_sub_u32_e32 v4, 0, v0
	v_and_b32_e32 v3, 0x3800, v1
	s_mov_b64 s[6:7], 0
	v_mov_b32_e32 v1, 0
	s_movk_i32 s15, 0xff7e
	s_movk_i32 s17, 0x80
	s_mov_b32 s18, 0
	s_barrier
	v_lshrrev_b32_e32 v4, 4, v0
	v_and_b32_e32 v5, 15, v0
	v_mul_u32_u24_e32 v4, 0x104, v4
	v_lshlrev_b32_e32 v5, 4, v5
	v_mov_b32_e32 v6, 0x4000400
	ds_write_b32 v4, v6 offset:16768
	s_waitcnt vmcnt(0)
	s_mov_b32 s0, 0xe0e0e0e0
	s_mov_b32 s1, 0x20202020
	s_mov_b32 s6, 0x01010101
	s_mov_b32 s7, 0x80808080
	v_and_b32_e32 v7, s0, v250
	v_xor_b32_e32 v7, s1, v7
	v_subrev_u32_e32 v9, s6, v7
	v_not_b32_e32 v7, v7
	v_and_b32_e32 v7, v9, v7
	v_and_b32_e32 v7, s7, v7
	v_and_b32_e32 v8, s0, v251
	v_xor_b32_e32 v8, s1, v8
	v_subrev_u32_e32 v9, s6, v8
	v_not_b32_e32 v8, v8
	v_and_b32_e32 v8, v9, v8
	v_and_b32_e32 v8, s7, v8
	v_or_b32_e32 v7, v7, v8
	v_bfe_u32 v8, v250, 0, 8
	v_bfe_u32 v9, v250, 8, 8
	v_min_u32_e32 v8, 64, v8
	v_min_u32_e32 v9, 64, v9
	v_lshlrev_b32_e32 v8, 4, v8
	v_lshlrev_b32_e32 v9, 20, v9
	v_or_b32_e32 v10, v8, v9
	v_bfe_u32 v8, v250, 16, 8
	v_bfe_u32 v9, v250, 24, 8
	v_min_u32_e32 v8, 64, v8
	v_min_u32_e32 v9, 64, v9
	v_lshlrev_b32_e32 v8, 4, v8
	v_lshlrev_b32_e32 v9, 20, v9
	v_or_b32_e32 v11, v8, v9
	v_bfe_u32 v8, v251, 0, 8
	v_bfe_u32 v9, v251, 8, 8
	v_min_u32_e32 v8, 64, v8
	v_min_u32_e32 v9, 64, v9
	v_lshlrev_b32_e32 v8, 4, v8
	v_lshlrev_b32_e32 v9, 20, v9
	v_or_b32_e32 v12, v8, v9
	v_bfe_u32 v8, v251, 16, 8
	v_bfe_u32 v9, v251, 24, 8
	v_min_u32_e32 v8, 64, v8
	v_min_u32_e32 v9, 64, v9
	v_lshlrev_b32_e32 v8, 4, v8
	v_lshlrev_b32_e32 v9, 20, v9
	v_or_b32_e32 v13, v8, v9
	s_cmp_eq_u32 s16, 0
	s_cbranch_scc0 .Ltok_bwd
	v_add_u32_e32 v4, v4, v5
	ds_write_b32 v4, v10 offset:16512
	ds_write_b32 v4, v11 offset:16516
	ds_write_b32 v4, v12 offset:16520
	ds_write_b32 v4, v13 offset:16524
	s_branch .Ltok_done

	.amdhsa_kernel _Z10gru_kernelPKhPf
		.amdhsa_group_segment_fixed_size 125728
		.amdhsa_private_segment_fixed_size 0
		.amdhsa_kernarg_size 16
		.amdhsa_user_sgpr_count 2
		.amdhsa_user_sgpr_dispatch_ptr 0
		.amdhsa_user_sgpr_queue_ptr 0
		.amdhsa_user_sgpr_kernarg_segment_ptr 1
		.amdhsa_user_sgpr_dispatch_id 0
		.amdhsa_user_sgpr_kernarg_preload_length 0
		.amdhsa_user_sgpr_kernarg_preload_offset 0
		.amdhsa_user_sgpr_private_segment_size 0
		.amdhsa_uses_dynamic_stack 0
		.amdhsa_enable_private_segment 0
		.amdhsa_system_sgpr_workgroup_id_x 1
		.amdhsa_system_sgpr_workgroup_id_y 0
		.amdhsa_system_sgpr_workgroup_id_z 0
		.amdhsa_system_sgpr_workgroup_info 0
		.amdhsa_system_vgpr_workitem_id 0
		.amdhsa_next_free_vgpr 252
		.amdhsa_next_free_sgpr 22
		.amdhsa_accum_offset 252
		.amdhsa_reserve_vcc 1
		.amdhsa_float_round_mode_32 0
		.amdhsa_float_round_mode_16_64 0
		.amdhsa_float_denorm_mode_32 3
		.amdhsa_float_denorm_mode_16_64 3
		.amdhsa_dx10_clamp 1
		.amdhsa_ieee_mode 1
		.amdhsa_fp16_overflow 0
		.amdhsa_tg_split 0
		.amdhsa_exception_fp_ieee_invalid_op 0
		.amdhsa_exception_fp_denorm_src 0
		.amdhsa_exception_fp_ieee_div_zero 0
		.amdhsa_exception_fp_ieee_overflow 0
		.amdhsa_exception_fp_ieee_underflow 0
		.amdhsa_exception_fp_ieee_inexact 0
		.amdhsa_exception_int_div_zero 0
	.end_amdhsa_kernel

.Lfunc_end1:
	.size	_Z10gru_kernelPKhPf, .Lfunc_end1-_Z10gru_kernelPKhPf
	.set _Z10gru_kernelPKhPf.num_vgpr, 252
	.set _Z10gru_kernelPKhPf.num_agpr, 0
	.set _Z10gru_kernelPKhPf.numbered_sgpr, 22
	.set _Z10gru_kernelPKhPf.num_named_barrier, 0
	.set _Z10gru_kernelPKhPf.private_seg_size, 0
	.set _Z10gru_kernelPKhPf.uses_vcc, 1
	.set _Z10gru_kernelPKhPf.uses_flat_scratch, 0
	.set _Z10gru_kernelPKhPf.has_dyn_sized_stack, 0
	.set _Z10gru_kernelPKhPf.has_recursion, 0
	.set _Z10gru_kernelPKhPf.has_indirect_call, 0

amdhsa.kernels:
  - .agpr_count:     0
    .args:
      - .actual_access:  read_only
        .address_space:  global
        .offset:         0
        .size:           8
        .value_kind:     global_buffer
      - .actual_access:  read_only
        .address_space:  global
        .offset:         8
        .size:           8
        .value_kind:     global_buffer
      - .actual_access:  read_only
        .address_space:  global
        .offset:         16
        .size:           8
        .value_kind:     global_buffer
      - .actual_access:  read_only
        .address_space:  global
        .offset:         24
        .size:           8
        .value_kind:     global_buffer
      - .actual_access:  read_only
        .address_space:  global
        .offset:         32
        .size:           8
        .value_kind:     global_buffer
      - .actual_access:  read_only
        .address_space:  global
        .offset:         40
        .size:           8
        .value_kind:     global_buffer
      - .actual_access:  read_only
        .address_space:  global
        .offset:         48
        .size:           8
        .value_kind:     global_buffer
      - .actual_access:  read_only
        .address_space:  global
        .offset:         56
        .size:           8
        .value_kind:     global_buffer
      - .actual_access:  read_only
        .address_space:  global
        .offset:         64
        .size:           8
        .value_kind:     global_buffer
      - .actual_access:  read_only
        .address_space:  global
        .offset:         72
        .size:           8
        .value_kind:     global_buffer
      - .actual_access:  read_only
        .address_space:  global
        .offset:         80
        .size:           8
        .value_kind:     global_buffer
      - .actual_access:  write_only
        .address_space:  global
        .offset:         88
        .size:           8
        .value_kind:     global_buffer
    .group_segment_fixed_size: 512
    .kernarg_segment_align: 8
    .kernarg_segment_size: 96
    .language:       OpenCL C
    .language_version:
      - 2
      - 0
    .max_flat_workgroup_size: 256
    .name:           _Z11prep_kernelPKiS0_PKfS2_S2_S2_S2_S2_S2_S2_S2_Ph
    .private_segment_fixed_size: 0
    .sgpr_count:     22
    .sgpr_spill_count: 0
    .symbol:         _Z11prep_kernelPKiS0_PKfS2_S2_S2_S2_S2_S2_S2_S2_Ph.kd
    .uniform_work_group_size: 1
    .uses_dynamic_stack: false
    .vgpr_count:     16
    .vgpr_spill_count: 0
    .wavefront_size: 64
  - .agpr_count:     0
    .args:
      - .actual_access:  read_only
        .address_space:  global
        .offset:         0
        .size:           8
        .value_kind:     global_buffer
      - .actual_access:  write_only
        .address_space:  global
        .offset:         8
        .size:           8
        .value_kind:     global_buffer
    .group_segment_fixed_size: 125728
    .kernarg_segment_align: 8
    .kernarg_segment_size: 16
    .language:       OpenCL C
    .language_version:
      - 2
      - 0
    .max_flat_workgroup_size: 512
    .name:           _Z10gru_kernelPKhPf
    .private_segment_fixed_size: 0
    .sgpr_count:     28
    .sgpr_spill_count: 0
    .symbol:         _Z10gru_kernelPKhPf.kd
    .uniform_work_group_size: 1
    .uses_dynamic_stack: false
    .vgpr_count:     252
    .vgpr_spill_count: 0
    .wavefront_size: 64
  - .agpr_count:     0
    .args:
      - .actual_access:  read_only
        .address_space:  global
        .offset:         0
        .size:           8
        .value_kind:     global_buffer
      - .actual_access:  read_only
        .address_space:  global
        .offset:         8
        .size:           8
        .value_kind:     global_buffer
      - .actual_access:  write_only
        .address_space:  global
        .offset:         16
        .size:           8
        .value_kind:     global_buffer
    .group_segment_fixed_size: 0
    .kernarg_segment_align: 8
    .kernarg_segment_size: 24
    .language:       OpenCL C
    .language_version:
      - 2
      - 0
    .max_flat_workgroup_size: 256
    .name:           _Z12final_kernelPKfS0_Pf
    .private_segment_fixed_size: 0
    .sgpr_count:     16
    .sgpr_spill_count: 0
    .symbol:         _Z12final_kernelPKfS0_Pf.kd
    .uniform_work_group_size: 1
    .uses_dynamic_stack: false
    .vgpr_count:     26
    .vgpr_spill_count: 0
    .wavefront_size: 64
